# v9 plus nt on read-once streams of P3 (gelu input rows) and the P4 token-mixing units (normalised rows, gelu-input tiles)
# baseline (speedup 1.0000x reference)
.LBB0_469:
	v_lshl_add_u64 v[20:21], s[10:11], 0, v[10:11]
	v_add_co_u32_e32 v20, vcc, 0x37c04000, v20
	global_load_dwordx4 v[2:5], v[12:13], off offset:16
	global_load_dwordx4 v[6:9], v[12:13], off
	v_addc_co_u32_e32 v21, vcc, 0, v21, vcc
	global_load_dwordx4 v[30:33], v[20:21], off nt
	global_load_dwordx4 v[34:37], v[20:21], off offset:1024 nt
	global_load_dwordx4 v[38:41], v[20:21], off offset:2048 nt
	global_load_dwordx4 v[42:45], v[20:21], off offset:3072 nt
	v_lshl_add_u64 v[18:19], s[6:7], 0, v[10:11]
	v_add_co_u32_e64 v18, s[0:1], s14, v18
	s_add_i32 s38, s38, s40
	s_nop 0
	v_addc_co_u32_e64 v19, s[0:1], 0, v19, s[0:1]
	s_add_u32 s6, s6, s8
	s_addc_u32 s7, s7, s9
	s_add_u32 s10, s10, s12
	s_addc_u32 s11, s11, s3
	s_cmpk_lt_i32 s38, 0x2000
	s_waitcnt vmcnt(3)
	v_and_b32_e32 v21, 0xffff0000, v30
	v_lshlrev_b32_e32 v20, 16, v30
	v_mul_f32_e32 v60, 0x3d372713, v21
	v_lshlrev_b32_e32 v29, 16, v31
	v_mul_f32_e32 v59, 0x3d372713, v20
	v_mul_f32_e32 v60, v60, v21
	v_and_b32_e32 v30, 0xffff0000, v31
	v_mul_f32_e32 v61, 0x3d372713, v29
	v_mul_f32_e32 v59, v59, v20
	v_fma_f32 v60, v60, v21, v21
	v_lshlrev_b32_e32 v31, 16, v32
	v_mul_f32_e32 v62, 0x3d372713, v30
	v_mul_f32_e32 v61, v61, v29
	v_fma_f32 v59, v59, v20, v20
	v_mul_f32_e32 v60, 0x3f4c422a, v60
	v_and_b32_e32 v32, 0xffff0000, v32
	v_mul_f32_e32 v63, 0x3d372713, v31
	v_mul_f32_e32 v62, v62, v30
	v_fma_f32 v61, v61, v29, v29
	v_mul_f32_e32 v59, 0x3f4c422a, v59
	v_mul_f32_e32 v60, -2.0, v60
	v_lshlrev_b32_e32 v46, 16, v33
	v_mul_f32_e32 v64, 0x3d372713, v32
	v_mul_f32_e32 v63, v63, v31
	v_fma_f32 v62, v62, v30, v30
	v_mul_f32_e32 v61, 0x3f4c422a, v61
	v_mul_f32_e32 v59, -2.0, v59
	v_mul_f32_e32 v60, 0x3fb8aa3b, v60
	v_and_b32_e32 v33, 0xffff0000, v33
	v_mul_f32_e32 v65, 0x3d372713, v46
	v_mul_f32_e32 v64, v64, v32
	v_fma_f32 v63, v63, v31, v31
	v_mul_f32_e32 v62, 0x3f4c422a, v62
	v_mul_f32_e32 v61, -2.0, v61
	v_mul_f32_e32 v59, 0x3fb8aa3b, v59
	v_exp_f32_e32 v60, v60
	s_waitcnt vmcnt(2)
	v_lshlrev_b32_e32 v47, 16, v34
	v_mul_f32_e32 v66, 0x3d372713, v33
	v_mul_f32_e32 v65, v65, v46
	v_fma_f32 v64, v64, v32, v32
	v_mul_f32_e32 v63, 0x3f4c422a, v63
	v_mul_f32_e32 v62, -2.0, v62
	v_mul_f32_e32 v61, 0x3fb8aa3b, v61
	v_exp_f32_e32 v59, v59
	v_and_b32_e32 v34, 0xffff0000, v34
	v_mul_f32_e32 v67, 0x3d372713, v47
	v_mul_f32_e32 v66, v66, v33
	v_fma_f32 v65, v65, v46, v46
	v_mul_f32_e32 v64, 0x3f4c422a, v64
	v_mul_f32_e32 v63, -2.0, v63
	v_mul_f32_e32 v62, 0x3fb8aa3b, v62
	v_exp_f32_e32 v61, v61
	v_lshlrev_b32_e32 v48, 16, v35
	v_mul_f32_e32 v68, 0x3d372713, v34
	v_mul_f32_e32 v67, v67, v47
	v_fma_f32 v66, v66, v33, v33
	v_mul_f32_e32 v65, 0x3f4c422a, v65
	v_mul_f32_e32 v64, -2.0, v64
	v_mul_f32_e32 v63, 0x3fb8aa3b, v63
	v_exp_f32_e32 v62, v62
	v_and_b32_e32 v35, 0xffff0000, v35
	v_mul_f32_e32 v69, 0x3d372713, v48
	v_mul_f32_e32 v68, v68, v34
	v_fma_f32 v67, v67, v47, v47
	v_mul_f32_e32 v66, 0x3f4c422a, v66
	v_mul_f32_e32 v65, -2.0, v65
	v_mul_f32_e32 v64, 0x3fb8aa3b, v64
	v_exp_f32_e32 v63, v63
	v_add_f32_e32 v60, 1.0, v60
	v_lshlrev_b32_e32 v49, 16, v36
	v_mul_f32_e32 v70, 0x3d372713, v35
	v_mul_f32_e32 v69, v69, v48
	v_fma_f32 v68, v68, v34, v34
	v_mul_f32_e32 v67, 0x3f4c422a, v67
	v_mul_f32_e32 v66, -2.0, v66
	v_mul_f32_e32 v65, 0x3fb8aa3b, v65
	v_exp_f32_e32 v64, v64
	v_add_f32_e32 v59, 1.0, v59
	v_rcp_f32_e32 v60, v60
	v_and_b32_e32 v36, 0xffff0000, v36
	v_mul_f32_e32 v71, 0x3d372713, v49
	v_mul_f32_e32 v70, v70, v35
	v_fma_f32 v69, v69, v48, v48
	v_mul_f32_e32 v68, 0x3f4c422a, v68
	v_mul_f32_e32 v67, -2.0, v67
	v_mul_f32_e32 v66, 0x3fb8aa3b, v66
	v_exp_f32_e32 v65, v65
	v_add_f32_e32 v61, 1.0, v61
	v_rcp_f32_e32 v59, v59
	v_lshlrev_b32_e32 v50, 16, v37
	v_mul_f32_e32 v72, 0x3d372713, v36
	v_mul_f32_e32 v71, v71, v49
	v_fma_f32 v70, v70, v35, v35
	v_mul_f32_e32 v69, 0x3f4c422a, v69
	v_mul_f32_e32 v68, -2.0, v68
	v_mul_f32_e32 v67, 0x3fb8aa3b, v67
	v_exp_f32_e32 v66, v66
	v_add_f32_e32 v62, 1.0, v62
	v_rcp_f32_e32 v61, v61
	v_and_b32_e32 v37, 0xffff0000, v37
	v_mul_f32_e32 v73, 0x3d372713, v50
	v_mul_f32_e32 v72, v72, v36
	v_fma_f32 v71, v71, v49, v49
	v_mul_f32_e32 v70, 0x3f4c422a, v70
	v_mul_f32_e32 v69, -2.0, v69
	v_mul_f32_e32 v68, 0x3fb8aa3b, v68
	v_exp_f32_e32 v67, v67
	v_add_f32_e32 v63, 1.0, v63
	v_rcp_f32_e32 v62, v62
	s_waitcnt vmcnt(1)
	v_lshlrev_b32_e32 v51, 16, v38
	v_mul_f32_e32 v74, 0x3d372713, v37
	v_mul_f32_e32 v73, v73, v50
	v_fma_f32 v72, v72, v36, v36
	v_mul_f32_e32 v71, 0x3f4c422a, v71
	v_mul_f32_e32 v70, -2.0, v70
	v_mul_f32_e32 v69, 0x3fb8aa3b, v69
	v_exp_f32_e32 v68, v68
	v_add_f32_e32 v64, 1.0, v64
	v_rcp_f32_e32 v63, v63
	v_mul_f32_e32 v21, v60, v21
	v_and_b32_e32 v38, 0xffff0000, v38
	v_mul_f32_e32 v75, 0x3d372713, v51
	v_mul_f32_e32 v74, v74, v37
	v_fma_f32 v73, v73, v50, v50
	v_mul_f32_e32 v72, 0x3f4c422a, v72
	v_mul_f32_e32 v71, -2.0, v71
	v_mul_f32_e32 v70, 0x3fb8aa3b, v70
	v_exp_f32_e32 v69, v69
	v_add_f32_e32 v65, 1.0, v65
	v_rcp_f32_e32 v64, v64
	v_mul_f32_e32 v20, v59, v20
	v_mul_f32_e32 v59, v21, v21
	v_lshlrev_b32_e32 v52, 16, v39
	v_mul_f32_e32 v76, 0x3d372713, v38
	v_mul_f32_e32 v75, v75, v51
	v_fma_f32 v74, v74, v37, v37
	v_mul_f32_e32 v73, 0x3f4c422a, v73
	v_mul_f32_e32 v72, -2.0, v72
	v_mul_f32_e32 v71, 0x3fb8aa3b, v71
	v_exp_f32_e32 v70, v70
	v_add_f32_e32 v66, 1.0, v66
	v_rcp_f32_e32 v65, v65
	v_mul_f32_e32 v29, v61, v29
	v_fmac_f32_e32 v59, v20, v20
	v_and_b32_e32 v39, 0xffff0000, v39
	v_mul_f32_e32 v77, 0x3d372713, v52
	v_mul_f32_e32 v76, v76, v38
	v_fma_f32 v75, v75, v51, v51
	v_mul_f32_e32 v74, 0x3f4c422a, v74
	v_mul_f32_e32 v73, -2.0, v73
	v_mul_f32_e32 v72, 0x3fb8aa3b, v72
	v_exp_f32_e32 v71, v71
	v_add_f32_e32 v67, 1.0, v67
	v_rcp_f32_e32 v66, v66
	v_mul_f32_e32 v30, v62, v30
	v_fmac_f32_e32 v59, v29, v29
	v_lshlrev_b32_e32 v53, 16, v40
	v_mul_f32_e32 v78, 0x3d372713, v39
	v_mul_f32_e32 v77, v77, v52
	v_fma_f32 v76, v76, v38, v38
	v_mul_f32_e32 v75, 0x3f4c422a, v75
	v_mul_f32_e32 v74, -2.0, v74
	v_mul_f32_e32 v73, 0x3fb8aa3b, v73
	v_exp_f32_e32 v72, v72
	v_add_f32_e32 v68, 1.0, v68
	v_rcp_f32_e32 v67, v67
	v_mul_f32_e32 v31, v63, v31
	v_fmac_f32_e32 v59, v30, v30
	v_and_b32_e32 v40, 0xffff0000, v40
	v_mul_f32_e32 v79, 0x3d372713, v53
	v_mul_f32_e32 v78, v78, v39
	v_fma_f32 v77, v77, v52, v52
	v_mul_f32_e32 v76, 0x3f4c422a, v76
	v_mul_f32_e32 v75, -2.0, v75
	v_mul_f32_e32 v74, 0x3fb8aa3b, v74
	v_exp_f32_e32 v73, v73
	v_add_f32_e32 v69, 1.0, v69
	v_rcp_f32_e32 v68, v68
	v_mul_f32_e32 v32, v64, v32
	v_fmac_f32_e32 v59, v31, v31
	v_lshlrev_b32_e32 v54, 16, v41
	v_mul_f32_e32 v80, 0x3d372713, v40
	v_mul_f32_e32 v79, v79, v53
	v_fma_f32 v78, v78, v39, v39
	v_mul_f32_e32 v77, 0x3f4c422a, v77
	v_mul_f32_e32 v76, -2.0, v76
	v_mul_f32_e32 v75, 0x3fb8aa3b, v75
	v_exp_f32_e32 v74, v74
	v_add_f32_e32 v70, 1.0, v70
	v_rcp_f32_e32 v69, v69
	v_mul_f32_e32 v46, v65, v46
	v_fmac_f32_e32 v59, v32, v32
	v_and_b32_e32 v41, 0xffff0000, v41
	v_mul_f32_e32 v81, 0x3d372713, v54
	v_mul_f32_e32 v80, v80, v40
	v_fma_f32 v79, v79, v53, v53
	v_mul_f32_e32 v78, 0x3f4c422a, v78
	v_mul_f32_e32 v77, -2.0, v77
	v_mul_f32_e32 v76, 0x3fb8aa3b, v76
	v_exp_f32_e32 v75, v75
	v_add_f32_e32 v71, 1.0, v71
	v_rcp_f32_e32 v70, v70
	v_mul_f32_e32 v33, v66, v33
	v_fmac_f32_e32 v59, v46, v46
	s_waitcnt vmcnt(0)
	v_lshlrev_b32_e32 v55, 16, v42
	v_mul_f32_e32 v82, 0x3d372713, v41
	v_mul_f32_e32 v81, v81, v54
	v_fma_f32 v80, v80, v40, v40
	v_mul_f32_e32 v79, 0x3f4c422a, v79
	v_mul_f32_e32 v78, -2.0, v78
	v_mul_f32_e32 v77, 0x3fb8aa3b, v77
	v_exp_f32_e32 v76, v76
	v_add_f32_e32 v72, 1.0, v72
	v_rcp_f32_e32 v71, v71
	v_mul_f32_e32 v47, v67, v47
	v_fmac_f32_e32 v59, v33, v33
	v_and_b32_e32 v42, 0xffff0000, v42
	v_mul_f32_e32 v83, 0x3d372713, v55
	v_mul_f32_e32 v82, v82, v41
	v_fma_f32 v81, v81, v54, v54
	v_mul_f32_e32 v80, 0x3f4c422a, v80
	v_mul_f32_e32 v79, -2.0, v79
	v_mul_f32_e32 v78, 0x3fb8aa3b, v78
	v_exp_f32_e32 v77, v77
	v_add_f32_e32 v73, 1.0, v73
	v_rcp_f32_e32 v72, v72
	v_mul_f32_e32 v34, v68, v34
	v_fmac_f32_e32 v59, v47, v47
	v_lshlrev_b32_e32 v56, 16, v43
	v_mul_f32_e32 v84, 0x3d372713, v42
	v_mul_f32_e32 v83, v83, v55
	v_fma_f32 v82, v82, v41, v41
	v_mul_f32_e32 v81, 0x3f4c422a, v81
	v_mul_f32_e32 v80, -2.0, v80
	v_mul_f32_e32 v79, 0x3fb8aa3b, v79
	v_exp_f32_e32 v78, v78
	v_add_f32_e32 v74, 1.0, v74
	v_rcp_f32_e32 v73, v73
	v_mul_f32_e32 v48, v69, v48
	v_fmac_f32_e32 v59, v34, v34
	v_and_b32_e32 v43, 0xffff0000, v43
	v_mul_f32_e32 v85, 0x3d372713, v56
	v_mul_f32_e32 v84, v84, v42
	v_fma_f32 v83, v83, v55, v55
	v_mul_f32_e32 v82, 0x3f4c422a, v82
	v_mul_f32_e32 v81, -2.0, v81
	v_mul_f32_e32 v80, 0x3fb8aa3b, v80
	v_exp_f32_e32 v79, v79
	v_add_f32_e32 v75, 1.0, v75
	v_rcp_f32_e32 v74, v74
	v_mul_f32_e32 v35, v70, v35
	v_fmac_f32_e32 v59, v48, v48
	v_lshlrev_b32_e32 v57, 16, v44
	v_mul_f32_e32 v86, 0x3d372713, v43
	v_mul_f32_e32 v85, v85, v56
	v_fma_f32 v84, v84, v42, v42
	v_mul_f32_e32 v83, 0x3f4c422a, v83
	v_mul_f32_e32 v82, -2.0, v82
	v_mul_f32_e32 v81, 0x3fb8aa3b, v81
	v_exp_f32_e32 v80, v80
	v_add_f32_e32 v76, 1.0, v76
	v_rcp_f32_e32 v75, v75
	v_mul_f32_e32 v49, v71, v49
	v_fmac_f32_e32 v59, v35, v35
	v_and_b32_e32 v44, 0xffff0000, v44
	v_mul_f32_e32 v87, 0x3d372713, v57
	v_mul_f32_e32 v86, v86, v43
	v_fma_f32 v85, v85, v56, v56
	v_mul_f32_e32 v84, 0x3f4c422a, v84
	v_mul_f32_e32 v83, -2.0, v83
	v_mul_f32_e32 v82, 0x3fb8aa3b, v82
	v_exp_f32_e32 v81, v81
	v_add_f32_e32 v77, 1.0, v77
	v_rcp_f32_e32 v76, v76
	v_mul_f32_e32 v36, v72, v36
	v_fmac_f32_e32 v59, v49, v49
	v_lshlrev_b32_e32 v58, 16, v45
	v_mul_f32_e32 v88, 0x3d372713, v44
	v_mul_f32_e32 v87, v87, v57
	v_fma_f32 v86, v86, v43, v43
	v_mul_f32_e32 v85, 0x3f4c422a, v85
	v_mul_f32_e32 v84, -2.0, v84
	v_mul_f32_e32 v83, 0x3fb8aa3b, v83
	v_exp_f32_e32 v82, v82
	v_add_f32_e32 v78, 1.0, v78
	v_rcp_f32_e32 v77, v77
	v_mul_f32_e32 v50, v73, v50
	v_fmac_f32_e32 v59, v36, v36
	v_and_b32_e32 v45, 0xffff0000, v45
	v_mul_f32_e32 v89, 0x3d372713, v58
	v_mul_f32_e32 v88, v88, v44
	v_fma_f32 v87, v87, v57, v57
	v_mul_f32_e32 v86, 0x3f4c422a, v86
	v_mul_f32_e32 v85, -2.0, v85
	v_mul_f32_e32 v84, 0x3fb8aa3b, v84
	v_exp_f32_e32 v83, v83
	v_add_f32_e32 v79, 1.0, v79
	v_rcp_f32_e32 v78, v78
	v_mul_f32_e32 v37, v74, v37
	v_fmac_f32_e32 v59, v50, v50
	v_mul_f32_e32 v90, 0x3d372713, v45
	v_mul_f32_e32 v89, v89, v58
	v_fma_f32 v88, v88, v44, v44
	v_mul_f32_e32 v87, 0x3f4c422a, v87
	v_mul_f32_e32 v86, -2.0, v86
	v_mul_f32_e32 v85, 0x3fb8aa3b, v85
	v_exp_f32_e32 v84, v84
	v_add_f32_e32 v80, 1.0, v80
	v_rcp_f32_e32 v79, v79
	v_mul_f32_e32 v51, v75, v51
	v_fmac_f32_e32 v59, v37, v37
	v_mul_f32_e32 v90, v90, v45
	v_fma_f32 v89, v89, v58, v58
	v_mul_f32_e32 v88, 0x3f4c422a, v88
	v_mul_f32_e32 v87, -2.0, v87
	v_mul_f32_e32 v86, 0x3fb8aa3b, v86
	v_exp_f32_e32 v85, v85
	v_add_f32_e32 v81, 1.0, v81
	v_rcp_f32_e32 v80, v80
	v_mul_f32_e32 v38, v76, v38
	v_fmac_f32_e32 v59, v51, v51
	v_fma_f32 v90, v90, v45, v45
	v_mul_f32_e32 v89, 0x3f4c422a, v89
	v_mul_f32_e32 v88, -2.0, v88
	v_mul_f32_e32 v87, 0x3fb8aa3b, v87
	v_exp_f32_e32 v86, v86
	v_add_f32_e32 v82, 1.0, v82
	v_rcp_f32_e32 v81, v81
	v_mul_f32_e32 v52, v77, v52
	v_fmac_f32_e32 v59, v38, v38
	v_mul_f32_e32 v90, 0x3f4c422a, v90
	v_mul_f32_e32 v89, -2.0, v89
	v_mul_f32_e32 v88, 0x3fb8aa3b, v88
	v_exp_f32_e32 v87, v87
	v_add_f32_e32 v83, 1.0, v83
	v_rcp_f32_e32 v82, v82
	v_mul_f32_e32 v39, v78, v39
	v_fmac_f32_e32 v59, v52, v52
	v_mul_f32_e32 v90, -2.0, v90
	v_mul_f32_e32 v89, 0x3fb8aa3b, v89
	v_exp_f32_e32 v88, v88
	v_add_f32_e32 v84, 1.0, v84
	v_rcp_f32_e32 v83, v83
	v_mul_f32_e32 v53, v79, v53
	v_fmac_f32_e32 v59, v39, v39
	v_mul_f32_e32 v90, 0x3fb8aa3b, v90
	v_exp_f32_e32 v89, v89
	v_add_f32_e32 v85, 1.0, v85
	v_rcp_f32_e32 v84, v84
	v_mul_f32_e32 v40, v80, v40
	v_fmac_f32_e32 v59, v53, v53
	v_exp_f32_e32 v90, v90
	v_add_f32_e32 v86, 1.0, v86
	v_rcp_f32_e32 v85, v85
	v_mul_f32_e32 v54, v81, v54
	v_fmac_f32_e32 v59, v40, v40
	v_add_f32_e32 v87, 1.0, v87
	v_rcp_f32_e32 v86, v86
	v_mul_f32_e32 v41, v82, v41
	v_fmac_f32_e32 v59, v54, v54
	v_add_f32_e32 v88, 1.0, v88
	v_rcp_f32_e32 v87, v87
	v_mul_f32_e32 v55, v83, v55
	v_fmac_f32_e32 v59, v41, v41
	v_add_f32_e32 v89, 1.0, v89
	v_rcp_f32_e32 v88, v88
	v_mul_f32_e32 v42, v84, v42
	v_fmac_f32_e32 v59, v55, v55
	v_add_f32_e32 v90, 1.0, v90
	v_rcp_f32_e32 v89, v89
	v_mul_f32_e32 v56, v85, v56
	v_fmac_f32_e32 v59, v42, v42
	v_rcp_f32_e32 v90, v90
	v_mul_f32_e32 v43, v86, v43
	v_fmac_f32_e32 v59, v56, v56
	v_mul_f32_e32 v57, v87, v57
	v_fmac_f32_e32 v59, v43, v43
	v_mul_f32_e32 v44, v88, v44
	v_fmac_f32_e32 v59, v57, v57
	v_mul_f32_e32 v58, v89, v58
	v_fmac_f32_e32 v59, v44, v44
	v_mul_f32_e32 v45, v90, v45
	v_fmac_f32_e32 v59, v58, v58
	v_fmac_f32_e32 v59, v45, v45
	ds_bpermute_b32 v60, v1, v59
	s_waitcnt lgkmcnt(0)
	v_add_f32_e32 v59, v59, v60
	ds_bpermute_b32 v60, v22, v59
	s_waitcnt lgkmcnt(0)
	v_add_f32_e32 v59, v59, v60
	ds_bpermute_b32 v60, v23, v59
	s_waitcnt lgkmcnt(0)
	v_add_f32_e32 v59, v59, v60
	ds_bpermute_b32 v60, v24, v59
	s_waitcnt lgkmcnt(0)
	v_add_f32_e32 v59, v59, v60
	ds_bpermute_b32 v60, v25, v59
	s_waitcnt lgkmcnt(0)
	v_add_f32_e32 v59, v59, v60
	ds_bpermute_b32 v60, v26, v59
	s_waitcnt lgkmcnt(0)
	v_add_f32_e32 v59, v59, v60
	v_fmamk_f32 v59, v59, 0x3a000000, v27
	v_mul_f32_e32 v60, 0x4f800000, v59
	v_cmp_gt_f32_e32 vcc, s13, v59
	s_nop 1
	v_cndmask_b32_e32 v59, v59, v60, vcc
	v_sqrt_f32_e32 v60, v59
	s_nop 0
	v_add_u32_e32 v61, -1, v60
	v_add_u32_e32 v62, 1, v60
	v_fma_f32 v63, -v61, v60, v59
	v_fma_f32 v64, -v62, v60, v59
	v_cmp_ge_f32_e64 s[0:1], 0, v63
	s_nop 1
	v_cndmask_b32_e64 v60, v60, v61, s[0:1]
	v_cmp_lt_f32_e64 s[0:1], 0, v64
	s_nop 1
	v_cndmask_b32_e64 v60, v60, v62, s[0:1]
	v_mul_f32_e32 v61, 0x37800000, v60
	v_cndmask_b32_e32 v60, v60, v61, vcc
	v_cmp_class_f32_e32 vcc, v59, v28
	s_nop 1
	v_cndmask_b32_e32 v59, v60, v59, vcc
	v_div_scale_f32 v60, s[0:1], v59, v59, 1.0
	v_rcp_f32_e32 v62, v60
	v_div_scale_f32 v61, vcc, 1.0, v59, 1.0
	v_fma_f32 v63, -v60, v62, 1.0
	v_fmac_f32_e32 v62, v63, v62
	v_mul_f32_e32 v63, v61, v62
	v_fma_f32 v64, -v60, v63, v61
	v_fmac_f32_e32 v63, v64, v62
	v_fma_f32 v60, -v60, v63, v61
	v_div_fmas_f32 v60, v60, v62, v63
	v_div_fixup_f32 v59, v60, v59, 1.0
	v_mul_f32_e32 v33, v33, v59
	v_mul_f32_e32 v20, v20, v59
	v_mul_f32_e32 v21, v21, v59
	v_mul_f32_e32 v29, v29, v59
	v_mul_f32_e32 v30, v30, v59
	v_mul_f32_e32 v31, v31, v59
	v_mul_f32_e32 v32, v32, v59
	v_mul_f32_e32 v46, v46, v59
	v_mul_f32_e32 v5, v5, v33
	v_mul_f32_e32 v6, v6, v20
	v_mul_f32_e32 v7, v7, v21
	v_mul_f32_e32 v8, v8, v29
	v_mul_f32_e32 v9, v9, v30
	v_mul_f32_e32 v20, v2, v31
	v_mul_f32_e32 v21, v3, v32
	v_mul_f32_e32 v29, v4, v46
	v_cvt_pk_bf16_f32 v2, v6, v7
	v_cvt_pk_bf16_f32 v3, v8, v9
	v_cvt_pk_bf16_f32 v4, v20, v21
	v_cvt_pk_bf16_f32 v5, v29, v5
	global_store_dwordx4 v[18:19], v[2:5], off
	global_load_dwordx4 v[2:5], v[12:13], off offset:2048
	s_nop 0
	global_load_dwordx4 v[6:9], v[12:13], off offset:2064
	v_mul_f32_e32 v20, v47, v59
	v_mul_f32_e32 v21, v34, v59
	v_mul_f32_e32 v29, v48, v59
	v_mul_f32_e32 v30, v35, v59
	v_mul_f32_e32 v31, v49, v59
	v_mul_f32_e32 v32, v36, v59
	v_mul_f32_e32 v33, v50, v59
	v_mul_f32_e32 v34, v37, v59
	s_waitcnt vmcnt(1)
	v_mul_f32_e32 v2, v2, v20
	v_mul_f32_e32 v3, v3, v21
	v_mul_f32_e32 v4, v4, v29
	v_mul_f32_e32 v5, v5, v30
	s_waitcnt vmcnt(0)
	v_mul_f32_e32 v6, v6, v31
	v_mul_f32_e32 v7, v7, v32
	v_mul_f32_e32 v8, v8, v33
	v_mul_f32_e32 v9, v9, v34
	v_cvt_pk_bf16_f32 v2, v2, v3
	v_cvt_pk_bf16_f32 v3, v4, v5
	v_cvt_pk_bf16_f32 v4, v6, v7
	v_cvt_pk_bf16_f32 v5, v8, v9
	global_store_dwordx4 v[18:19], v[2:5], off offset:1024
	global_load_dwordx4 v[2:5], v[14:15], off
	s_nop 0
	global_load_dwordx4 v[6:9], v[14:15], off offset:16
	v_mul_f32_e32 v20, v51, v59
	v_mul_f32_e32 v21, v38, v59
	v_mul_f32_e32 v29, v52, v59
	v_mul_f32_e32 v30, v39, v59
	v_mul_f32_e32 v31, v53, v59
	v_mul_f32_e32 v32, v40, v59
	v_mul_f32_e32 v33, v54, v59
	v_mul_f32_e32 v34, v41, v59
	s_waitcnt vmcnt(1)
	v_mul_f32_e32 v2, v2, v20
	v_mul_f32_e32 v3, v3, v21
	v_mul_f32_e32 v4, v4, v29
	v_mul_f32_e32 v5, v5, v30
	s_waitcnt vmcnt(0)
	v_mul_f32_e32 v6, v6, v31
	v_mul_f32_e32 v7, v7, v32
	v_mul_f32_e32 v8, v8, v33
	v_mul_f32_e32 v9, v9, v34
	v_cvt_pk_bf16_f32 v2, v2, v3
	v_cvt_pk_bf16_f32 v3, v4, v5
	v_cvt_pk_bf16_f32 v4, v6, v7
	v_cvt_pk_bf16_f32 v5, v8, v9
	global_store_dwordx4 v[18:19], v[2:5], off offset:2048
	global_load_dwordx4 v[2:5], v[16:17], off
	s_nop 0
	global_load_dwordx4 v[6:9], v[16:17], off offset:16
	v_mul_f32_e32 v20, v55, v59
	v_mul_f32_e32 v21, v42, v59
	v_mul_f32_e32 v29, v56, v59
	v_mul_f32_e32 v30, v43, v59
	v_mul_f32_e32 v31, v57, v59
	v_mul_f32_e32 v32, v44, v59
	v_mul_f32_e32 v33, v58, v59
	v_mul_f32_e32 v34, v45, v59
	s_waitcnt vmcnt(1)
	v_mul_f32_e32 v2, v2, v20
	v_mul_f32_e32 v3, v3, v21
	v_mul_f32_e32 v4, v4, v29
	v_mul_f32_e32 v5, v5, v30
	s_waitcnt vmcnt(0)
	v_mul_f32_e32 v6, v6, v31
	v_mul_f32_e32 v7, v7, v32
	v_mul_f32_e32 v8, v8, v33
	v_mul_f32_e32 v9, v9, v34
	v_cvt_pk_bf16_f32 v2, v2, v3
	v_cvt_pk_bf16_f32 v3, v4, v5
	v_cvt_pk_bf16_f32 v4, v6, v7
	v_cvt_pk_bf16_f32 v5, v8, v9
	global_store_dwordx4 v[18:19], v[2:5], off offset:3072
	s_cbranch_scc1 .LBB0_469

.LBB0_554:
	s_andn2_b64 vcc, exec, s[6:7]
	s_cbranch_vccnz .LBB0_616
	s_and_b32 s3, s2, 7
	s_cmpk_gt_i32 s2, 0x7f
	s_mov_b64 s[6:7], -1
	s_cbranch_scc0 .LBB0_594
	s_cmpk_gt_u32 s2, 0x27f
	s_cbranch_scc1 .LBB0_574
	s_add_i32 s14, s2, 0xffffff80
	s_lshr_b32 s12, s14, 7
	s_mov_b32 s13, 0
	s_waitcnt vmcnt(0)
	v_mov_b32_e32 v1, v0
	s_lshl_b64 s[6:7], s[12:13], 11
	s_lshl_b32 s12, s14, 4
	s_waitcnt lgkmcnt(0)
	s_add_i32 s44, s2, 0x3c0
	v_lshlrev_b32_e32 v4, 4, v1
	s_and_b32 s12, s12, 0x780
	v_ashrrev_i32_e32 v2, 4, v1
	v_and_b32_e32 v162, 0xf0, v4
	v_add_u32_e32 v4, 0x200, v1
	v_add_u32_e32 v6, 0x400, v1
	v_add_u32_e32 v1, 0x600, v1
	s_or_b32 s6, s6, s12
	s_lshl_b32 s12, s44, 9
	v_ashrrev_i32_e32 v8, 4, v1
	s_and_b32 s12, s12, 0xe00
	v_ashrrev_i32_e32 v4, 4, v4
	v_ashrrev_i32_e32 v6, 4, v6
	v_ashrrev_i32_e32 v9, 31, v8
	s_add_u32 s14, s58, s12
	v_ashrrev_i32_e32 v3, 31, v2
	v_ashrrev_i32_e32 v5, 31, v4
	v_ashrrev_i32_e32 v7, 31, v6
	v_lshl_add_u64 v[8:9], s[6:7], 0, v[8:9]
	s_addc_u32 s15, s59, 0
	v_lshl_add_u64 v[2:3], s[6:7], 0, v[2:3]
	v_lshl_add_u64 v[4:5], s[6:7], 0, v[4:5]
	v_lshl_add_u64 v[6:7], s[6:7], 0, v[6:7]
	v_lshlrev_b64 v[8:9], 12, v[8:9]
	v_lshlrev_b64 v[2:3], 12, v[2:3]
	v_mov_b32_e32 v163, 0
	v_lshlrev_b64 v[4:5], 12, v[4:5]
	v_lshlrev_b64 v[6:7], 12, v[6:7]
	v_lshl_add_u64 v[8:9], s[14:15], 0, v[8:9]
	v_lshl_add_u64 v[2:3], s[14:15], 0, v[2:3]
	v_lshl_add_u64 v[4:5], s[14:15], 0, v[4:5]
	v_lshl_add_u64 v[6:7], s[14:15], 0, v[6:7]
	v_lshl_add_u64 v[8:9], v[8:9], 0, v[162:163]
	v_lshl_add_u64 v[2:3], v[2:3], 0, v[162:163]
	v_lshl_add_u64 v[4:5], v[4:5], 0, v[162:163]
	v_lshl_add_u64 v[6:7], v[6:7], 0, v[162:163]
	global_load_dwordx4 v[58:61], v[8:9], off offset:256 nt
	global_load_dwordx4 v[82:85], v[8:9], off nt
	global_load_dwordx4 v[70:73], v[6:7], off offset:256 nt
	global_load_dwordx4 v[78:81], v[6:7], off nt
	global_load_dwordx4 v[66:69], v[4:5], off offset:256 nt
	global_load_dwordx4 v[74:77], v[4:5], off nt
	global_load_dwordx4 v[62:65], v[2:3], off offset:256 nt
	global_load_dwordx4 v[54:57], v[2:3], off nt
	s_lshl_b32 s6, s3, 16
	s_add_u32 s14, s80, s6
	s_addc_u32 s15, s81, 0
	s_lshl_b32 s6, s3, 8
	s_lshl_b32 s45, s3, 7
	s_add_i32 s45, s45, s54
	s_lshl_b32 s46, s2, 4
	s_add_i32 s47, s66, 0x3c000
	s_sub_i32 s48, 0xfffffbc0, s2
	s_add_i32 s49, s2, 0x440
	s_add_i32 s66, 0, 0x10000
	s_movk_i32 s67, 0x7000
	s_lshl_b32 s16, s6, 1
	s_mov_b64 s[38:39], 0x3000
	s_movk_i32 s68, 0x3000
	s_mov_b32 s69, 0x8000
	s_movk_i32 s70, 0x2000
	s_mov_b64 s[40:41], 0x1000
	s_movk_i32 s71, 0x1000
	s_mov_b32 s78, 0x5040100
	s_movk_i32 s79, 0x4000
	s_movk_i32 s80, 0x6000
	s_mov_b32 s81, 0xa000
	s_mov_b32 s84, 0xc000
	s_mov_b32 s85, 0xe000
	v_mov_b32_e32 v1, 0x7000
	v_mov_b32_e32 v196, 0x3f80
	s_mov_b32 s86, s2
	s_branch .LBB0_560

.LBB0_562:
	v_bfe_u32 v86, v201, 4, 2
	v_cndmask_b32_e64 v52, 0, 1, s[42:43]
	v_mov_b32_e32 v208, 0
	v_cmp_ne_u32_e64 s[6:7], 1, v52
	s_andn2_b64 vcc, exec, s[42:43]
	v_lshlrev_b32_e32 v162, 3, v86
	v_or_b32_e32 v52, s54, v200
	s_waitcnt lgkmcnt(0)
	s_barrier
	s_cbranch_vccnz .LBB0_564
	s_add_i32 s12, s86, 0xffffff80
	s_lshr_b32 s12, s12, 7
	s_lshl_b64 s[30:31], s[12:13], 11
	s_add_i32 s12, s46, 0xfffff800
	s_and_b32 s12, s12, 0x780
	s_add_i32 s12, s12, s54
	v_mov_b32_e32 v53, v163
	s_add_u32 s12, s30, s12
	v_lshlrev_b64 v[2:3], 9, v[52:53]
	v_or_b32_e32 v53, s12, v200
	v_mov_b64_e32 v[88:89], s[8:9]
	s_addc_u32 s17, s31, 0
	v_mad_u64_u32 v[88:89], s[30:31], v53, s67, v[88:89]
	v_mad_u32_u24 v89, s17, v1, v89
	s_mov_b32 s17, s13
	v_lshl_add_u64 v[88:89], v[88:89], 0, s[16:17]
	v_lshl_add_u64 v[2:3], s[14:15], 0, v[2:3]
	v_lshlrev_b32_e32 v4, 5, v86
	v_mov_b32_e32 v5, v163
	v_lshl_add_u64 v[88:89], v[88:89], 0, v[162:163]
	v_lshl_add_u64 v[34:35], v[2:3], 0, v[4:5]
	v_lshl_add_u64 v[90:91], v[88:89], 0, s[38:39]
	v_add_co_u32_e32 v88, vcc, s68, v88
	global_load_dwordx4 v[2:5], v[34:35], off offset:16
	global_load_dwordx4 v[6:9], v[34:35], off
	global_load_dwordx4 v[10:13], v[34:35], off offset:144
	global_load_dwordx4 v[14:17], v[34:35], off offset:128
	global_load_dwordx4 v[18:21], v[34:35], off offset:272
	global_load_dwordx4 v[22:25], v[34:35], off offset:256
	global_load_dwordx4 v[30:33], v[34:35], off offset:400
	s_nop 0
	global_load_dwordx4 v[34:37], v[34:35], off offset:384
	v_addc_co_u32_e32 v89, vcc, 0, v89, vcc
	global_load_dwordx2 v[186:187], v[90:91], off offset:32 nt
	global_load_dwordx2 v[184:185], v[90:91], off offset:64 nt
	global_load_dwordx2 v[182:183], v[90:91], off offset:96 nt
	global_load_dwordx2 v[180:181], v[90:91], off offset:128 nt
	global_load_dwordx2 v[178:179], v[90:91], off offset:160 nt
	global_load_dwordx2 v[176:177], v[90:91], off offset:192 nt
	global_load_dwordx2 v[174:175], v[90:91], off offset:224 nt
	global_load_dwordx2 v[172:173], v[90:91], off offset:256 nt
	global_load_dwordx2 v[170:171], v[90:91], off offset:288 nt
	global_load_dwordx2 v[168:169], v[90:91], off offset:320 nt
	global_load_dwordx2 v[166:167], v[90:91], off offset:352 nt
	global_load_dwordx2 v[164:165], v[90:91], off offset:384 nt
	global_load_dwordx2 v[194:195], v[88:89], off nt
	global_load_dwordx2 v[192:193], v[90:91], off offset:416 nt
	global_load_dwordx2 v[190:191], v[90:91], off offset:448 nt
	global_load_dwordx2 v[188:189], v[90:91], off offset:480 nt
	v_or_b32_e32 v88, s45, v200
	v_mov_b32_e32 v89, v163
	v_lshl_add_u64 v[88:89], v[88:89], 2, s[82:83]
	global_load_dword v208, v[88:89], off
.LBB0_564:
	s_cmpk_gt_i32 s87, 0x5bf
	s_cbranch_scc1 .LBB0_569
	v_mov_b32_e32 v53, v0
	s_cmpk_gt_i32 s87, 0x3bf
	s_mov_b64 s[42:43], -1
	s_cbranch_scc0 .LBB0_567
	s_lshr_b32 s12, s86, 7
	s_lshl_b64 s[30:31], s[12:13], 11
	s_and_b32 s12, s46, 0x780
	s_or_b32 s30, s30, s12
	s_add_i32 s12, s47, 0x8000
	s_and_b32 s12, s12, 0x700
	v_ashrrev_i32_e32 v54, 4, v53
	s_lshl_b32 s12, s12, 1
	v_ashrrev_i32_e32 v55, 31, v54
	s_add_u32 s34, s58, s12
	v_lshl_add_u64 v[54:55], s[30:31], 0, v[54:55]
	s_addc_u32 s35, s59, 0
	v_lshlrev_b64 v[54:55], 12, v[54:55]
	v_lshlrev_b32_e32 v56, 4, v53
	v_lshl_add_u64 v[54:55], s[34:35], 0, v[54:55]
	v_and_b32_e32 v56, 0xf0, v56
	v_mov_b32_e32 v57, v163
	v_lshl_add_u64 v[58:59], v[54:55], 0, v[56:57]
	v_add_u32_e32 v54, 0x200, v53
	v_ashrrev_i32_e32 v54, 4, v54
	v_ashrrev_i32_e32 v55, 31, v54
	v_lshl_add_u64 v[54:55], s[30:31], 0, v[54:55]
	v_lshlrev_b64 v[54:55], 12, v[54:55]
	v_lshl_add_u64 v[54:55], s[34:35], 0, v[54:55]
	v_lshl_add_u64 v[60:61], v[54:55], 0, v[56:57]
	v_add_u32_e32 v54, 0x400, v53
	v_ashrrev_i32_e32 v54, 4, v54
	v_ashrrev_i32_e32 v55, 31, v54
	v_lshl_add_u64 v[54:55], s[30:31], 0, v[54:55]
	v_lshlrev_b64 v[54:55], 12, v[54:55]
	v_lshl_add_u64 v[54:55], s[34:35], 0, v[54:55]
	v_lshl_add_u64 v[70:71], v[54:55], 0, v[56:57]
	v_add_u32_e32 v54, 0x600, v53
	v_ashrrev_i32_e32 v54, 4, v54
	v_ashrrev_i32_e32 v55, 31, v54
	v_lshl_add_u64 v[54:55], s[30:31], 0, v[54:55]
	v_lshlrev_b64 v[54:55], 12, v[54:55]
	v_lshl_add_u64 v[54:55], s[34:35], 0, v[54:55]
	v_lshl_add_u64 v[88:89], v[54:55], 0, v[56:57]
	global_load_dwordx4 v[54:57], v[58:59], off nt
	global_load_dwordx4 v[62:65], v[58:59], off offset:256 nt
	global_load_dwordx4 v[74:77], v[60:61], off nt
	global_load_dwordx4 v[66:69], v[60:61], off offset:256 nt
	global_load_dwordx4 v[78:81], v[70:71], off nt
	s_nop 0
	global_load_dwordx4 v[70:73], v[70:71], off offset:256 nt
	s_nop 0
	global_load_dwordx4 v[82:85], v[88:89], off nt
	global_load_dwordx4 v[58:61], v[88:89], off offset:256 nt
	s_mov_b64 s[42:43], 0
.LBB0_567:
	s_andn2_b64 vcc, exec, s[42:43]
	s_cbranch_vccnz .LBB0_569
	s_mul_hi_u32 s12, s49, 0xf0f0f0f1
	s_lshr_b32 s12, s12, 4
	s_add_i32 s42, s86, 0x440
	s_mul_i32 s12, s12, 17
	s_add_i32 s17, s48, s12
	s_mul_hi_u32 s18, s42, 0xf0f0f0f1
	s_sub_i32 s12, s86, s12
	s_lshr_b32 s19, s18, 4
	s_add_i32 s43, s12, 0x43e
	s_add_i32 s89, s12, 0x440
	s_bfe_u32 s90, s18, 0x10004
	s_lshr_b32 s12, s18, 8
	s_bfe_u32 s92, s18, 0x30005
	s_cmp_lt_i32 s89, 2
	s_cselect_b64 s[30:31], -1, 0
	s_and_b64 s[34:35], s[30:31], exec
	s_cselect_b32 s35, 1, 17
	s_cselect_b32 s34, s89, s43
	s_add_i32 s35, s35, s17
	s_cmp_eq_u32 s90, 0
	s_cselect_b32 s17, s34, s35
	s_lshl_b64 s[34:35], s[12:13], 11
	s_and_b32 s12, s18, 0xffffff00
	s_addk_i32 s12, 0x2000
	s_and_b64 s[90:91], s[30:31], exec
	s_cselect_b32 s18, 0, s35
	s_cselect_b32 s12, s12, s34
	s_lshl_b32 s34, s17, 7
	s_ashr_i32 s35, s34, 31
	s_add_u32 s34, s12, s34
	s_addc_u32 s35, s18, s35
	s_add_i32 s12, s17, 2
	s_and_b64 s[30:31], s[30:31], exec
	s_mul_i32 s19, s19, 18
	s_cselect_b32 s12, s17, s12
	s_add_i32 s12, s12, s19
	s_mul_hi_i32 s17, s12, 0x600
	s_mulk_i32 s12, 0x600
	s_add_u32 s30, s52, s12
	v_lshlrev_b32_e32 v26, 4, v53
	s_addc_u32 s31, s53, s17
	s_lshl_b32 s12, s92, 8
	s_waitcnt vmcnt(7)
	v_and_b32_e32 v54, 0xf0, v26
	v_ashrrev_i32_e32 v26, 4, v53
	s_add_u32 s90, s56, s12
	v_ashrrev_i32_e32 v27, 31, v26
	s_addc_u32 s91, s57, 0
	v_mov_b32_e32 v55, v163
	v_lshl_add_u64 v[56:57], s[34:35], 0, v[26:27]
	v_lshl_add_u64 v[46:47], s[90:91], 0, v[54:55]
	v_lshlrev_b64 v[28:29], 11, v[56:57]
	v_lshl_add_u64 v[28:29], v[46:47], 0, v[28:29]
	v_lshl_add_u64 v[38:39], v[26:27], 2, s[30:31]
	global_load_dwordx4 v[26:29], v[28:29], off nt
	s_nop 0
	global_load_dword v51, v[38:39], off offset:512
	v_add_u32_e32 v38, 0x200, v53
	v_ashrrev_i32_e32 v38, 4, v38
	v_ashrrev_i32_e32 v39, 31, v38
	s_waitcnt vmcnt(2)
	v_lshl_add_u64 v[58:59], s[34:35], 0, v[38:39]
	v_lshlrev_b64 v[40:41], 11, v[58:59]
	v_lshl_add_u64 v[40:41], v[46:47], 0, v[40:41]
	v_lshl_add_u64 v[42:43], v[38:39], 2, s[30:31]
	global_load_dwordx4 v[38:41], v[40:41], off nt
	s_nop 0
	global_load_dword v197, v[42:43], off offset:512
	v_add_u32_e32 v42, 0x400, v53
	v_ashrrev_i32_e32 v42, 4, v42
	v_ashrrev_i32_e32 v43, 31, v42
	v_lshl_add_u64 v[60:61], s[34:35], 0, v[42:43]
	v_lshlrev_b64 v[44:45], 11, v[60:61]
	v_lshl_add_u64 v[44:45], v[46:47], 0, v[44:45]
	v_lshl_add_u64 v[48:49], v[42:43], 2, s[30:31]
	global_load_dwordx4 v[42:45], v[44:45], off nt
	s_nop 0
	global_load_dword v198, v[48:49], off offset:512
	v_add_u32_e32 v48, 0x600, v53
	v_ashrrev_i32_e32 v48, 4, v48
	v_ashrrev_i32_e32 v49, 31, v48
	v_lshl_add_u64 v[62:63], s[34:35], 0, v[48:49]
	v_lshlrev_b64 v[64:65], 11, v[62:63]
	s_mov_b32 s43, s13
	v_lshl_add_u64 v[46:47], v[46:47], 0, v[64:65]
	v_lshl_add_u64 v[64:65], v[48:49], 2, s[30:31]
	s_lshl_b64 s[30:31], s[42:43], 2
	s_add_u32 s30, s0, s30
	global_load_dwordx4 v[46:49], v[46:47], off nt
	s_nop 0
	global_load_dword v199, v[64:65], off offset:512
	s_addc_u32 s31, s1, s31
	v_mov_b64_e32 v[64:65], s[8:9]
	global_load_dword v50, v163, s[30:31]
	v_mad_u64_u32 v[66:67], s[30:31], v56, s67, v[64:65]
	v_mad_i32_i24 v67, v57, s67, v67
	s_lshl_b32 s12, s92, 9
	v_lshl_add_u64 v[56:57], v[66:67], 0, s[12:13]
	v_mad_u64_u32 v[68:69], s[30:31], v58, s67, v[64:65]
	v_lshl_add_u64 v[56:57], v[56:57], 0, v[54:55]
	v_mad_i32_i24 v69, v59, s67, v69
	v_lshl_add_u64 v[66:67], v[56:57], 0, s[40:41]
	v_add_co_u32_e32 v56, vcc, s71, v56
	v_lshl_add_u64 v[58:59], v[68:69], 0, s[12:13]
	v_mad_u64_u32 v[70:71], s[30:31], v60, s67, v[64:65]
	v_addc_co_u32_e32 v57, vcc, 0, v57, vcc
	v_lshl_add_u64 v[58:59], v[58:59], 0, v[54:55]
	v_mad_i32_i24 v71, v61, s67, v71
	v_lshl_add_u64 v[68:69], v[58:59], 0, s[40:41]
	v_add_co_u32_e32 v58, vcc, s71, v58
	v_lshl_add_u64 v[60:61], v[70:71], 0, s[12:13]
	v_mad_u64_u32 v[64:65], s[30:31], v62, s67, v[64:65]
	v_addc_co_u32_e32 v59, vcc, 0, v59, vcc
	v_lshl_add_u64 v[60:61], v[60:61], 0, v[54:55]
	v_mad_i32_i24 v65, v63, s67, v65
	v_lshl_add_u64 v[70:71], v[60:61], 0, s[40:41]
	v_add_co_u32_e32 v60, vcc, s71, v60
	v_lshl_add_u64 v[62:63], v[64:65], 0, s[12:13]
	s_nop 0
	v_addc_co_u32_e32 v61, vcc, 0, v61, vcc
	v_lshl_add_u64 v[54:55], v[62:63], 0, v[54:55]
	v_add_co_u32_e32 v82, vcc, 0x1000, v54
	v_lshl_add_u64 v[88:89], v[54:55], 0, s[40:41]
	s_nop 0
	v_addc_co_u32_e32 v83, vcc, 0, v55, vcc
	global_load_dwordx4 v[54:57], v[56:57], off nt
	s_nop 0
	global_load_dwordx4 v[62:65], v[66:67], off offset:256 nt
	global_load_dwordx4 v[74:77], v[58:59], off nt
	s_nop 0
	global_load_dwordx4 v[66:69], v[68:69], off offset:256 nt
	s_nop 0
	global_load_dwordx4 v[78:81], v[60:61], off nt
	s_nop 0
	global_load_dwordx4 v[70:73], v[70:71], off offset:256 nt
	s_nop 0
	global_load_dwordx4 v[82:85], v[82:83], off nt
	s_nop 0
	global_load_dwordx4 v[58:61], v[88:89], off offset:256 nt
